# baseline (speedup 1.0000x reference)
.LBB1_1:
	v_mfma_f32_32x32x64_f8f6f4 v[76:91], v[84:91], v[116:123], v[36:51]
	v_cvt_pk_fp8_f32 v132, v161, v163
	v_add_u32_e32 v68, s36, v176
	v_cvt_pk_fp8_f32 v132, v162, v164 op_sel:[0,0,1]
	ds_read_b128 v[162:165], v68 offset:49152
	ds_read_b128 v[166:169], v68 offset:50176
	v_cvt_pk_fp8_f32 v133, v150, v154
	v_cvt_pk_fp8_f32 v133, v152, v157 op_sel:[0,0,1]
	s_lshl_b32 s16, s12, 12
	s_add_i32 s15, s16, 0x3000
	s_add_i32 s17, s14, s33
	s_mov_b32 m0, s17
	s_nop 0
	buffer_load_dwordx4 v174, s[20:23], s15 offen lds
	v_cvt_pk_fp8_f32 v134, v149, v153
	v_cvt_pk_fp8_f32 v134, v151, v156 op_sel:[0,0,1]
	v_cvt_pk_fp8_f32 v135, v155, v159
	v_cvt_pk_fp8_f32 v135, v158, v160 op_sel:[0,0,1]
	v_cvt_pk_fp8_f32 v136, v100, v148
	v_cvt_pk_fp8_f32 v136, v101, v102 op_sel:[0,0,1]
	s_waitcnt lgkmcnt(2)
	v_mfma_f32_32x32x64_f8f6f4 v[92:107], v[92:99], v[116:123], v[36:51]
	ds_read_b128 v[148:151], v68 offset:49664
	ds_read_b128 v[152:155], v68 offset:50688
	v_cvt_pk_fp8_f32 v137, v143, v146
	v_cvt_pk_fp8_f32 v137, v145, v147 op_sel:[0,0,1]
	s_add_i32 s15, s16, 0x1000
	s_add_i32 s17, s13, s34
	s_mov_b32 m0, s17
	s_nop 0
	buffer_load_dwordx4 v174, s[24:27], s15 offen lds
	v_cvt_pk_fp8_f32 v138, v69, v109
	v_cvt_pk_fp8_f32 v138, v108, v142 op_sel:[0,0,1]
	v_cvt_pk_fp8_f32 v139, v110, v144
	v_cvt_pk_fp8_f32 v139, v111, v114 op_sel:[0,0,1]
	s_waitcnt lgkmcnt(2)
	s_nop 0
	v_mfma_f32_32x32x64_f8f6f4 v[4:19], v[162:169], v[132:139], v[4:19]
	v_exp_f32_e32 v142, v76
	v_exp_f32_e32 v143, v77
	v_exp_f32_e32 v144, v78
	v_exp_f32_e32 v145, v79
	v_exp_f32_e32 v146, v80
	v_exp_f32_e32 v147, v81
	v_exp_f32_e32 v156, v82
	v_exp_f32_e32 v157, v83
	v_add_u32_e32 v158, s13, v176
	ds_read_b128 v[108:111], v158
	ds_read_b128 v[112:115], v158 offset:1024
	ds_read_b128 v[52:55], v158 offset:512
	ds_read_b128 v[56:59], v158 offset:1536
	v_exp_f32_e32 v159, v84
	v_exp_f32_e32 v160, v85
	v_mfma_f32_16x16x128_f8f6f4 v[200:203], v[124:131], v[132:139], v[200:203]
	v_exp_f32_e32 v161, v86
	v_exp_f32_e32 v162, v87
	v_exp_f32_e32 v163, v88
	v_exp_f32_e32 v164, v89
	v_exp_f32_e32 v165, v90
	v_exp_f32_e32 v166, v91
	s_waitcnt lgkmcnt(4)
	v_mfma_f32_32x32x64_f8f6f4 v[20:35], v[148:155], v[132:139], v[20:35]
	v_exp_f32_e32 v167, v92
	v_exp_f32_e32 v168, v93
	v_exp_f32_e32 v169, v94
	v_exp_f32_e32 v170, v95
	v_exp_f32_e32 v148, v96
	v_exp_f32_e32 v149, v97
	v_exp_f32_e32 v150, v98
	v_exp_f32_e32 v151, v99
	v_exp_f32_e32 v152, v100
	v_exp_f32_e32 v153, v101
	v_exp_f32_e32 v154, v102
	v_exp_f32_e32 v155, v103
	v_exp_f32_e32 v158, v104
	v_exp_f32_e32 v171, v105
	v_exp_f32_e32 v177, v106
	v_exp_f32_e32 v186, v107
	s_add_i32 s15, s13, 0x4000
	s_cmpk_lg_u32 s13, 0x8000
	s_cselect_b32 s15, s15, 0
	s_waitcnt vmcnt(2) lgkmcnt(0)
	s_barrier
	v_mfma_f32_32x32x64_f8f6f4 v[84:99], v[108:115], v[116:123], v[36:51]
	v_cvt_pk_fp8_f32 v132, v142, v143
	v_add_u32_e32 v142, s14, v176
	v_cvt_pk_fp8_f32 v132, v144, v145 op_sel:[0,0,1]
	ds_read_b128 v[60:63], v142 offset:49152
	ds_read_b128 v[64:67], v142 offset:50176
	v_cvt_pk_fp8_f32 v133, v146, v147
	v_cvt_pk_fp8_f32 v133, v156, v157 op_sel:[0,0,1]
	s_add_i32 s14, s16, 0x4000
	s_add_i32 s17, s13, s33
	s_mov_b32 m0, s17
	s_nop 0
	buffer_load_dwordx4 v174, s[20:23], s14 offen lds
	v_cvt_pk_fp8_f32 v134, v159, v160
	v_cvt_pk_fp8_f32 v134, v161, v162 op_sel:[0,0,1]
	v_cvt_pk_fp8_f32 v135, v163, v164
	v_cvt_pk_fp8_f32 v135, v165, v166 op_sel:[0,0,1]
	s_waitcnt lgkmcnt(2)
	v_mfma_f32_32x32x64_f8f6f4 v[100:115], v[52:59], v[116:123], v[36:51]
	v_cvt_pk_fp8_f32 v136, v167, v168
	v_cvt_pk_fp8_f32 v136, v169, v170 op_sel:[0,0,1]
	ds_read_b128 v[178:181], v142 offset:49664
	ds_read_b128 v[182:185], v142 offset:50688
	v_cvt_pk_fp8_f32 v137, v148, v149
	v_cvt_pk_fp8_f32 v137, v150, v151 op_sel:[0,0,1]
	s_addk_i32 s16, 0x2000
	s_add_i32 s14, s15, s34
	s_mov_b32 m0, s14
	s_nop 0
	buffer_load_dwordx4 v174, s[24:27], s16 offen lds
	v_cvt_pk_fp8_f32 v138, v152, v153
	v_cvt_pk_fp8_f32 v138, v154, v155 op_sel:[0,0,1]
	v_cvt_pk_fp8_f32 v139, v158, v171
	v_cvt_pk_fp8_f32 v139, v177, v186 op_sel:[0,0,1]
	v_sub_f32_e32 v52, v200, v204
	v_mov_b32_e32 v204, v200
	v_max_f32_e32 v0, v0, v0
	v_max_f32_e32 v0, v0, v52
	s_waitcnt lgkmcnt(2)
	v_mfma_f32_32x32x64_f8f6f4 v[4:19], v[60:67], v[132:139], v[4:19]
	v_exp_f32_e32 v161, v84
	v_exp_f32_e32 v163, v85
	v_exp_f32_e32 v162, v86
	v_exp_f32_e32 v164, v87
	v_exp_f32_e32 v150, v88
	v_exp_f32_e32 v154, v89
	v_exp_f32_e32 v152, v90
	v_exp_f32_e32 v157, v91
	v_add_u32_e32 v141, s15, v176
	ds_read_b128 v[84:87], v141
	ds_read_b128 v[88:91], v141 offset:1024
	v_mfma_f32_16x16x128_f8f6f4 v[200:203], v[124:131], v[132:139], v[200:203]
	v_exp_f32_e32 v149, v92
	v_exp_f32_e32 v153, v93
	v_exp_f32_e32 v151, v94
	v_exp_f32_e32 v156, v95
	v_exp_f32_e32 v155, v96
	v_exp_f32_e32 v159, v97
	v_exp_f32_e32 v158, v98
	v_exp_f32_e32 v160, v99
	ds_read_b128 v[92:95], v141 offset:512
	ds_read_b128 v[96:99], v141 offset:1536
	s_waitcnt lgkmcnt(4)
	v_mfma_f32_32x32x64_f8f6f4 v[20:35], v[178:185], v[132:139], v[20:35]
	v_exp_f32_e32 v100, v100
	v_exp_f32_e32 v148, v101
	v_exp_f32_e32 v101, v102
	v_exp_f32_e32 v102, v103
	v_exp_f32_e32 v143, v104
	v_exp_f32_e32 v146, v105
	v_exp_f32_e32 v145, v106
	v_exp_f32_e32 v147, v107
	v_exp_f32_e32 v69, v108
	v_exp_f32_e32 v109, v109
	v_exp_f32_e32 v108, v110
	v_exp_f32_e32 v142, v111
	v_exp_f32_e32 v110, v112
	v_exp_f32_e32 v144, v113
	v_exp_f32_e32 v111, v114
	v_exp_f32_e32 v114, v115
	s_add_i32 s16, s15, 0x4000
	s_cmpk_lg_u32 s15, 0x8000
	s_mov_b32 s36, s13
	s_mov_b32 s14, s15
	s_cselect_b32 s13, s16, 0
	s_add_i32 s12, s12, 2
	s_cmp_gt_u32 s12, 26
	s_waitcnt vmcnt(2) lgkmcnt(0)
	s_barrier
	s_cbranch_scc0 .LBB1_1
	v_add_u32_e32 v113, 0xc000, v176
	v_mov_b32_e32 v112, 0x7f7f7f7f
	v_cvt_pk_fp8_f32 v132, v161, v163
	v_cvt_pk_fp8_f32 v132, v162, v164 op_sel:[0,0,1]
	s_waitcnt lgkmcnt(2)
	v_mfma_f32_32x32x64_f8f6f4 v[70:85], v[84:91], v[116:123], v[36:51]
	ds_read_b128 v[162:165], v113 offset:32768
	ds_read_b128 v[166:169], v113 offset:33792
	v_cvt_pk_fp8_f32 v133, v150, v154
	v_cvt_pk_fp8_f32 v133, v152, v157 op_sel:[0,0,1]
	s_mov_b32 s13, 0x1e000
	s_mov_b32 m0, s33
	s_nop 0
	buffer_load_dwordx4 v174, s[20:23], s13 offen lds
	v_cvt_pk_fp8_f32 v134, v149, v153
	v_cvt_pk_fp8_f32 v134, v151, v156 op_sel:[0,0,1]
	v_cvt_pk_fp8_f32 v135, v155, v159
	v_cvt_pk_fp8_f32 v135, v158, v160 op_sel:[0,0,1]
	v_cvt_pk_fp8_f32 v136, v100, v148
	v_cvt_pk_fp8_f32 v136, v101, v102 op_sel:[0,0,1]
	s_waitcnt lgkmcnt(2)
	v_mfma_f32_32x32x64_f8f6f4 v[86:101], v[92:99], v[116:123], v[36:51]
	ds_read_b128 v[148:151], v113 offset:33280
	ds_read_b128 v[152:155], v113 offset:34304
	v_cvt_pk_fp8_f32 v137, v143, v146
	v_cvt_pk_fp8_f32 v137, v145, v147 op_sel:[0,0,1]
	s_cmp_lg_u32 0, -1
	s_cselect_b32 s12, 0, 0
	s_add_i32 s15, s12, s35
	s_add_i32 s12, s15, 0x10000
	s_mov_b32 s26, s22
	s_mov_b32 s27, s23
	s_mov_b32 s14, 0x1c000
	s_mov_b32 m0, s12
	s_nop 0
	buffer_load_dwordx4 v174, s[24:27], s14 offen lds
	s_and_b32 s41, s2, 3
	s_lshl_b32 s42, s41, 6
	s_lshl_b32 s43, s3, 5
	s_add_i32 s42, s42, s43
	v_add_u32_e32 v198, s42, v172
	v_lshlrev_b32_e32 v198, 8, v198
	v_lshl_add_u32 v198, v175, 4, v198
	s_lshl_b32 s44, s41, 8
	s_lshl_b32 s45, s3, 7
	s_add_i32 s44, s44, s45
	v_lshl_add_u32 v199, v175, 4, s44
	s_lshl_b32 s46, s41, 2
	v_mov_b32_e32 v205, s46
	global_load_dwordx4 v[208:211], v198, s[4:5]
	global_load_dwordx4 v[212:215], v198, s[4:5] offset:32
	global_load_dwordx4 v[216:219], v198, s[4:5] offset:64
	global_load_dwordx4 v[220:223], v198, s[4:5] offset:96
	global_load_dwordx4 v[224:227], v198, s[4:5] offset:128
	v_cvt_pk_fp8_f32 v138, v69, v109
	v_cvt_pk_fp8_f32 v138, v108, v142 op_sel:[0,0,1]
	v_cvt_pk_fp8_f32 v139, v110, v144
	v_cvt_pk_fp8_f32 v139, v111, v114 op_sel:[0,0,1]
	s_waitcnt lgkmcnt(2)
	s_nop 0
	v_mfma_f32_32x32x64_f8f6f4 v[4:19], v[162:169], v[132:139], v[4:19]
	v_exp_f32_e32 v104, v73
	v_exp_f32_e32 v69, v70
	v_exp_f32_e32 v102, v71
	v_exp_f32_e32 v103, v72
	v_exp_f32_e32 v110, v74
	v_exp_f32_e32 v111, v75
	v_exp_f32_e32 v114, v76
	v_exp_f32_e32 v115, v77
	ds_read_b128 v[70:73], v176 offset:16384
	ds_read_b128 v[74:77], v176 offset:17408
	v_mfma_f32_16x16x128_f8f6f4 v[200:203], v[124:131], v[132:139], v[200:203]
	v_exp_f32_e32 v140, v78
	v_exp_f32_e32 v141, v79
	v_exp_f32_e32 v142, v80
	v_exp_f32_e32 v143, v81
	v_exp_f32_e32 v144, v82
	v_exp_f32_e32 v145, v83
	v_exp_f32_e32 v146, v84
	v_exp_f32_e32 v147, v85
	s_waitcnt lgkmcnt(2)
	v_mfma_f32_32x32x64_f8f6f4 v[20:35], v[148:155], v[132:139], v[20:35]
	v_exp_f32_e32 v156, v86
	v_exp_f32_e32 v157, v87
	v_exp_f32_e32 v158, v88
	v_exp_f32_e32 v159, v89
	v_exp_f32_e32 v148, v90
	v_exp_f32_e32 v149, v91
	v_exp_f32_e32 v150, v92
	v_exp_f32_e32 v151, v93
	ds_read_b128 v[86:89], v176 offset:16896
	ds_read_b128 v[90:93], v176 offset:17920
	v_exp_f32_e32 v152, v94
	v_exp_f32_e32 v153, v95
	v_exp_f32_e32 v154, v96
	v_exp_f32_e32 v155, v97
	v_exp_f32_e32 v160, v98
	v_exp_f32_e32 v161, v99
	v_exp_f32_e32 v162, v100
	v_exp_f32_e32 v163, v101
	s_waitcnt vmcnt(7) lgkmcnt(0)
	s_barrier
	s_waitcnt lgkmcnt(2)
	v_mfma_f32_32x32x64_f8f6f4 v[70:85], v[70:77], v[116:123], v[36:51]
	v_cvt_pk_fp8_f32 v132, v69, v102
	v_cvt_pk_fp8_f32 v132, v103, v104 op_sel:[0,0,1]
	ds_read_b128 v[102:105], v176 offset:49152
	ds_read_b128 v[106:109], v176 offset:50176
	v_cvt_pk_fp8_f32 v133, v110, v111
	v_cvt_pk_fp8_f32 v133, v114, v115 op_sel:[0,0,1]
	s_add_i32 s16, s15, 0x4000
	s_mov_b32 s14, 0x1f000
	s_mov_b32 m0, s16
	s_nop 0
	buffer_load_dwordx4 v174, s[20:23], s14 offen lds
	v_cvt_pk_fp8_f32 v134, v140, v141
	v_cvt_pk_fp8_f32 v134, v142, v143 op_sel:[0,0,1]
	v_cvt_pk_fp8_f32 v135, v144, v145
	v_cvt_pk_fp8_f32 v135, v146, v147 op_sel:[0,0,1]
	s_waitcnt lgkmcnt(2)
	v_mfma_f32_32x32x64_f8f6f4 v[86:101], v[86:93], v[116:123], v[36:51]
	v_cvt_pk_fp8_f32 v136, v156, v157
	v_cvt_pk_fp8_f32 v136, v158, v159 op_sel:[0,0,1]
	ds_read_b128 v[140:143], v176 offset:49664
	ds_read_b128 v[144:147], v176 offset:50688
	v_cvt_pk_fp8_f32 v137, v148, v149
	v_cvt_pk_fp8_f32 v137, v150, v151 op_sel:[0,0,1]
	s_add_i32 s15, s15, 0x14000
	s_mov_b32 s16, 0x1d000
	s_mov_b32 m0, s15
	s_nop 0
	buffer_load_dwordx4 v174, s[24:27], s16 offen lds
	global_load_dwordx4 v[228:231], v198, s[4:5] offset:160
	global_load_dwordx4 v[232:235], v198, s[4:5] offset:192
	global_load_dwordx4 v[236:239], v198, s[4:5] offset:224
	global_load_dwordx4 v[240:243], v199, s[6:7]
	v_cvt_pk_fp8_f32 v138, v152, v153
	v_cvt_pk_fp8_f32 v138, v154, v155 op_sel:[0,0,1]
	v_cvt_pk_fp8_f32 v139, v160, v161
	v_cvt_pk_fp8_f32 v139, v162, v163 op_sel:[0,0,1]
	v_sub_f32_e32 v114, v200, v204
	v_mov_b32_e32 v204, v200
	s_waitcnt lgkmcnt(2)
	v_mfma_f32_32x32x64_f8f6f4 v[4:19], v[102:109], v[132:139], v[4:19]
	v_exp_f32_e32 v110, v70
	v_exp_f32_e32 v111, v71
	v_exp_f32_e32 v148, v73
	v_exp_f32_e32 v115, v72
	v_exp_f32_e32 v149, v74
	v_exp_f32_e32 v150, v75
	v_exp_f32_e32 v151, v76
	v_exp_f32_e32 v152, v77
	ds_read_b128 v[70:73], v176 offset:32768
	ds_read_b128 v[74:77], v176 offset:33792
	v_mfma_f32_16x16x128_f8f6f4 v[200:203], v[124:131], v[132:139], v[200:203]
	v_exp_f32_e32 v153, v78
	v_exp_f32_e32 v154, v79
	v_exp_f32_e32 v155, v80
	v_exp_f32_e32 v156, v81
	v_exp_f32_e32 v157, v83
	v_exp_f32_e32 v158, v84
	v_exp_f32_e32 v159, v85
	s_nop 7
	v_exp_f32_e32 v53, v82
	s_waitcnt lgkmcnt(2)
	v_mfma_f32_32x32x64_f8f6f4 v[20:35], v[140:147], v[132:139], v[20:35]
	v_exp_f32_e32 v160, v86
	v_exp_f32_e32 v161, v87
	v_exp_f32_e32 v162, v88
	v_exp_f32_e32 v163, v89
	v_exp_f32_e32 v164, v90
	v_exp_f32_e32 v165, v91
	v_exp_f32_e32 v166, v92
	v_exp_f32_e32 v167, v93
	ds_read_b128 v[78:81], v176 offset:33280
	ds_read_b128 v[82:85], v176 offset:34304
	v_exp_f32_e32 v168, v94
	v_exp_f32_e32 v169, v95
	v_exp_f32_e32 v170, v96
	v_exp_f32_e32 v171, v97
	v_exp_f32_e32 v177, v98
	v_exp_f32_e32 v178, v99
	v_exp_f32_e32 v179, v100
	v_exp_f32_e32 v180, v101
	s_waitcnt vmcnt(11) lgkmcnt(0)
	s_barrier
	s_waitcnt lgkmcnt(2)
	v_mfma_f32_32x32x64_f8f6f4 v[86:101], v[70:77], v[116:123], v[36:51]
	v_cvt_pk_fp8_f32 v132, v110, v111
	v_cvt_pk_fp8_f32 v132, v115, v148 op_sel:[0,0,1]
	ds_read_b128 v[102:105], v113 offset:16384
	ds_read_b128 v[106:109], v113 offset:17408
	v_cvt_pk_fp8_f32 v133, v149, v150
	v_cvt_pk_fp8_f32 v133, v151, v152 op_sel:[0,0,1]
	v_cvt_pk_fp8_f32 v134, v153, v154
	v_cvt_pk_fp8_f32 v134, v155, v156 op_sel:[0,0,1]
	v_cvt_pk_fp8_f32 v135, v53, v157
	v_cvt_pk_fp8_f32 v135, v158, v159 op_sel:[0,0,1]
	s_waitcnt lgkmcnt(2)
	v_mfma_f32_32x32x64_f8f6f4 v[70:85], v[78:85], v[116:123], v[36:51]
	v_cvt_pk_fp8_f32 v136, v160, v161
	v_cvt_pk_fp8_f32 v136, v162, v163 op_sel:[0,0,1]
	ds_read_b128 v[140:143], v113 offset:16896
	ds_read_b128 v[144:147], v113 offset:17920
	v_cvt_pk_fp8_f32 v137, v164, v165
	v_cvt_pk_fp8_f32 v137, v166, v167 op_sel:[0,0,1]
	s_mov_b32 m0, s34
	s_nop 0
	buffer_load_dwordx4 v174, s[24:27], s13 offen lds
	global_load_dwordx4 v[244:247], v199, s[6:7] offset:32
	global_load_dwordx4 v[248:251], v199, s[6:7] offset:64
	global_load_dwordx4 v[252:255], v199, s[6:7] offset:96
	global_load_dword v205, v205, s[8:9]
	v_cvt_pk_fp8_f32 v138, v168, v169
	v_cvt_pk_fp8_f32 v138, v170, v171 op_sel:[0,0,1]
	v_cvt_pk_fp8_f32 v139, v177, v178
	v_cvt_pk_fp8_f32 v139, v179, v180 op_sel:[0,0,1]
	s_waitcnt lgkmcnt(2)
	s_nop 0
	v_mfma_f32_32x32x64_f8f6f4 v[4:19], v[102:109], v[132:139], v[4:19]
	v_exp_f32_e32 v148, v88
	v_exp_f32_e32 v149, v89
	v_exp_f32_e32 v53, v86
	v_exp_f32_e32 v115, v87
	v_exp_f32_e32 v150, v92
	v_exp_f32_e32 v151, v93
	v_exp_f32_e32 v102, v90
	v_exp_f32_e32 v103, v91
	ds_read_b128 v[86:89], v176
	ds_read_b128 v[90:93], v176 offset:1024
	v_mfma_f32_16x16x128_f8f6f4 v[200:203], v[124:131], v[132:139], v[200:203]
	v_exp_f32_e32 v152, v94
	v_exp_f32_e32 v153, v95
	v_exp_f32_e32 v154, v96
	v_exp_f32_e32 v155, v97
	v_exp_f32_e32 v156, v98
	v_exp_f32_e32 v157, v99
	v_exp_f32_e32 v158, v100
	v_exp_f32_e32 v159, v101
	s_waitcnt lgkmcnt(2)
	v_mfma_f32_32x32x64_f8f6f4 v[20:35], v[140:147], v[132:139], v[20:35]
	v_exp_f32_e32 v160, v70
	v_exp_f32_e32 v161, v71
	v_exp_f32_e32 v162, v72
	v_exp_f32_e32 v163, v73
	v_exp_f32_e32 v164, v74
	v_exp_f32_e32 v165, v75
	v_exp_f32_e32 v166, v76
	v_exp_f32_e32 v167, v77
	ds_read_b128 v[94:97], v176 offset:512
	ds_read_b128 v[98:101], v176 offset:1536
	v_exp_f32_e32 v168, v78
	v_exp_f32_e32 v169, v79
	v_exp_f32_e32 v170, v80
	v_exp_f32_e32 v171, v81
	v_exp_f32_e32 v177, v82
	v_exp_f32_e32 v178, v83
	v_exp_f32_e32 v179, v84
	v_exp_f32_e32 v180, v85
	s_waitcnt vmcnt(9) lgkmcnt(0)
	s_barrier
	s_waitcnt lgkmcnt(2)
	v_mfma_f32_32x32x64_f8f6f4 v[70:85], v[86:93], v[116:123], v[36:51]
	ds_read_b128 v[104:107], v113 offset:32768
	ds_read_b128 v[108:111], v113 offset:33792
	v_cvt_pk_fp8_f32 v132, v53, v115
	v_cvt_pk_fp8_f32 v133, v102, v103
	v_cvt_pk_fp8_f32 v134, v152, v153
	v_cvt_pk_fp8_f32 v132, v148, v149 op_sel:[0,0,1]
	v_cvt_pk_fp8_f32 v133, v150, v151 op_sel:[0,0,1]
	v_cvt_pk_fp8_f32 v134, v154, v155 op_sel:[0,0,1]
	v_cvt_pk_fp8_f32 v135, v156, v157
	v_cvt_pk_fp8_f32 v135, v158, v159 op_sel:[0,0,1]
	s_waitcnt lgkmcnt(2)
	v_mfma_f32_32x32x64_f8f6f4 v[86:101], v[94:101], v[116:123], v[36:51]
	v_cvt_pk_fp8_f32 v136, v160, v161
	v_cvt_pk_fp8_f32 v136, v162, v163 op_sel:[0,0,1]
	ds_read_b128 v[140:143], v113 offset:33280
	ds_read_b128 v[144:147], v113 offset:34304
	v_cvt_pk_fp8_f32 v137, v164, v165
	v_cvt_pk_fp8_f32 v137, v166, v167 op_sel:[0,0,1]
	s_mov_b32 m0, s12
	s_nop 0
	buffer_load_dwordx4 v174, s[24:27], s14 offen lds
	v_cvt_pk_fp8_f32 v138, v168, v169
	v_cvt_pk_fp8_f32 v138, v170, v171 op_sel:[0,0,1]
	v_cvt_pk_fp8_f32 v139, v177, v178
	v_cvt_pk_fp8_f32 v139, v179, v180 op_sel:[0,0,1]
	v_sub_f32_e32 v52, v200, v204
	v_mov_b32_e32 v204, v200
	v_max3_f32 v0, v0, v114, v52
	v_exp_f32_e32 v72, v72
	v_exp_f32_e32 v73, v73
	v_exp_f32_e32 v52, v70
	v_exp_f32_e32 v53, v71
	v_exp_f32_e32 v102, v74
	v_exp_f32_e32 v103, v75
	v_exp_f32_e32 v114, v76
	v_exp_f32_e32 v115, v77
	ds_read_b128 v[150:153], v176 offset:16384
	ds_read_b128 v[154:157], v176 offset:17408
	v_mfma_f32_16x16x128_f8f6f4 v[200:203], v[124:131], v[132:139], v[200:203]
	v_exp_f32_e32 v177, v78
	v_exp_f32_e32 v178, v79
	v_exp_f32_e32 v179, v80
	v_exp_f32_e32 v180, v81
	s_nop 10
	v_exp_f32_e32 v55, v82
	v_exp_f32_e32 v181, v83
	v_exp_f32_e32 v182, v84
	v_exp_f32_e32 v183, v85
	v_exp_f32_e32 v184, v86
	v_exp_f32_e32 v185, v87
	v_exp_f32_e32 v88, v88
	v_exp_f32_e32 v89, v89
	v_exp_f32_e32 v186, v90
	v_exp_f32_e32 v187, v91
	v_exp_f32_e32 v188, v92
	v_exp_f32_e32 v189, v93
	ds_read_b128 v[164:167], v176 offset:16896
	ds_read_b128 v[168:171], v176 offset:17920
	v_exp_f32_e32 v190, v94
	v_exp_f32_e32 v191, v95
	v_exp_f32_e32 v192, v96
	v_exp_f32_e32 v193, v97
	v_exp_f32_e32 v194, v98
	v_exp_f32_e32 v195, v99
	v_exp_f32_e32 v196, v100
	v_exp_f32_e32 v197, v101
	s_waitcnt vmcnt(0) lgkmcnt(0)
	s_barrier
	v_mov_b32_e32 v148, v132
	v_cvt_pk_fp8_f32 v148, v52, v53
	v_cvt_pk_fp8_f32 v148, v72, v73 op_sel:[0,0,1]
	s_waitcnt lgkmcnt(2)
	v_mfma_f32_32x32x64_f8f6f4 v[72:87], v[150:157], v[116:123], v[36:51]
	ds_read_b128 v[156:159], v176 offset:49152
	ds_read_b128 v[160:163], v176 offset:50176
	v_mov_b32_e32 v149, v133
	v_cvt_pk_fp8_f32 v149, v102, v103
	v_cvt_pk_fp8_f32 v149, v114, v115 op_sel:[0,0,1]
	v_mov_b32_e32 v150, v134
	v_cvt_pk_fp8_f32 v150, v177, v178
	v_cvt_pk_fp8_f32 v150, v179, v180 op_sel:[0,0,1]
	v_mov_b32_e32 v151, v135
	v_cvt_pk_fp8_f32 v151, v55, v181
	v_cvt_pk_fp8_f32 v151, v182, v183 op_sel:[0,0,1]
	v_mov_b32_e32 v152, v136
	v_cvt_pk_fp8_f32 v152, v184, v185
	v_cvt_pk_fp8_f32 v152, v88, v89 op_sel:[0,0,1]
	s_waitcnt lgkmcnt(2)
	v_mfma_f32_32x32x64_f8f6f4 v[88:103], v[164:171], v[116:123], v[36:51]
	ds_read_b128 v[164:167], v176 offset:49664
	ds_read_b128 v[168:171], v176 offset:50688
	v_mov_b32_e32 v153, v137
	v_cvt_pk_fp8_f32 v153, v186, v187
	v_cvt_pk_fp8_f32 v153, v188, v189 op_sel:[0,0,1]
	v_mov_b32_e32 v154, v138
	v_cvt_pk_fp8_f32 v154, v190, v191
	v_cvt_pk_fp8_f32 v154, v192, v193 op_sel:[0,0,1]
	v_mov_b32_e32 v155, v139
	v_cvt_pk_fp8_f32 v155, v194, v195
	v_cvt_pk_fp8_f32 v155, v196, v197 op_sel:[0,0,1]
	v_sub_f32_e32 v52, v200, v204
	v_mov_b32_e32 v204, v200
	s_nop 2
	v_exp_f32_e32 v36, v72
	v_exp_f32_e32 v37, v73
	v_exp_f32_e32 v38, v74
	v_exp_f32_e32 v39, v75
	v_exp_f32_e32 v40, v76
	v_exp_f32_e32 v41, v77
	v_exp_f32_e32 v42, v78
	v_exp_f32_e32 v43, v79
	v_exp_f32_e32 v53, v80
	v_exp_f32_e32 v80, v83
	v_exp_f32_e32 v54, v81
	v_exp_f32_e32 v55, v82
	v_exp_f32_e32 v81, v84
	v_exp_f32_e32 v82, v85
	v_exp_f32_e32 v83, v86
	v_exp_f32_e32 v84, v87
	v_exp_f32_e32 v44, v88
	v_exp_f32_e32 v45, v89
	v_exp_f32_e32 v46, v90
	v_exp_f32_e32 v47, v91
	v_exp_f32_e32 v48, v92
	v_exp_f32_e32 v49, v93
	v_exp_f32_e32 v50, v94
	v_exp_f32_e32 v51, v95
	v_exp_f32_e32 v75, v96
	v_exp_f32_e32 v85, v97
	v_exp_f32_e32 v86, v98
	v_exp_f32_e32 v87, v99
	v_exp_f32_e32 v88, v100
	v_exp_f32_e32 v89, v101
	v_exp_f32_e32 v90, v102
	v_exp_f32_e32 v91, v103
	v_mov_b32_e32 v72, 0
	v_mov_b32_e32 v76, 0
	v_mov_b32_e32 v73, 0
	v_mov_b32_e32 v77, 0
	v_cvt_pk_fp8_f32 v72, v36, v37
	v_cvt_pk_fp8_f32 v76, v44, v45
	v_cvt_pk_fp8_f32 v73, v40, v41
	v_cvt_pk_fp8_f32 v77, v48, v49
	v_cvt_pk_fp8_f32 v72, v38, v39 op_sel:[0,0,1]
	v_cvt_pk_fp8_f32 v76, v46, v47 op_sel:[0,0,1]
	v_cvt_pk_fp8_f32 v73, v42, v43 op_sel:[0,0,1]
	v_cvt_pk_fp8_f32 v77, v50, v51 op_sel:[0,0,1]
	v_mfma_f32_16x16x128_f8f6f4 v[200:203], v[124:131], v[148:155], v[200:203]
	v_mov_b32_e32 v78, 0
	v_mov_b32_e32 v79, 0
	v_mov_b32_e32 v74, 0
	v_cvt_pk_fp8_f32 v78, v75, v85
	v_mov_b32_e32 v75, 0
	v_cvt_pk_fp8_f32 v74, v53, v54
	v_cvt_pk_fp8_f32 v75, v81, v82
	v_cvt_pk_fp8_f32 v79, v88, v89
	v_cvt_pk_fp8_f32 v78, v86, v87 op_sel:[0,0,1]
	v_cvt_pk_fp8_f32 v74, v55, v80 op_sel:[0,0,1]
	v_cvt_pk_fp8_f32 v75, v83, v84 op_sel:[0,0,1]
	v_cvt_pk_fp8_f32 v79, v90, v91 op_sel:[0,0,1]
	ds_read_b128 v[80:83], v113 offset:16384
	s_nop 1
	ds_read_b128 v[58:61], v113 offset:16896
	ds_read_b128 v[84:87], v113 offset:17408
	ds_read_b128 v[62:65], v113 offset:17920
	s_mov_b32 s12, 0x43c80000
	v_mfma_f32_16x16x128_f8f6f4 v[200:203], v[124:131], v[72:79], v[200:203]
	s_nop 15
	s_nop 3
	v_sub_f32_e32 v37, v200, v204
	v_max3_f32 v0, v0, v52, v37
	v_cmp_nge_f32_e32 vcc, s12, v0
	s_cmp_lg_u64 vcc, 0
	s_cselect_b64 s[12:13], -1, 0
	s_cbranch_vccz .LBB1_12
	v_mfma_f32_32x32x64_f8f6f4 v[4:19], v[104:111], v[132:139], v[4:19]
	s_andn2_b64 vcc, exec, s[12:13]
	v_mfma_f32_32x32x64_f8f6f4 v[20:35], v[140:147], v[132:139], v[20:35]
	s_cbranch_vccnz .LBB1_5
